# P10 epilogue: two staging rounds of 2 row-group pairs (second pair in idle ring slots) instead of four rounds: 4 workgroup barriers per unit instead of 8
# baseline (speedup 1.0000x reference)
; #define LAS __attribute__((address_space(3)))
; __device__ __forceinline__ unsigned pk4_fp8(float a, float b, float c, float d) { int w = 0; w = __builtin_amdgcn_cvt_pk_fp8_f32(a, b, w, false); w = __builtin_amdgcn_cvt_pk_fp8_f32(c, d, w, true); return (unsigned)w; }
;     __device__ __forceinline__ void operator()(const f32x4 (&acc)[2][2][4][2], const Unit& u, int wr, int wc, int fr, int fq) const {
;         const int e = u.pn / npn, pnl = u.pn - e * npn; const int tid = threadIdx.x;
;         const int col0 = pnl * BM + wc * 32 + 8 * fq;
;         f32x4 bv[2][2];
; #pragma unroll
;         for (int bj = 0; bj < 2; ++bj)
; #pragma unroll
;             for (int n = 0; n < 2; ++n) bv[bj][n] = *(const f32x4*)(bias + (size_t)e * bias_ld + col0 + bj * HALF + 4 * n);
;         constexpr int PITCH = 272, SLAB = 32 * PITCH;
;         LAS unsigned char* wp = stg + (16 * wr + fr) * PITCH + 32 * wc + 8 * fq;
;         const int rr = tid >> 4, cc = tid & 15; const LAS unsigned char* rp = stg + rr * PITCH + cc * 16;
;         unsigned char* gp = O + (size_t)(u.pm * BM + 64 * (rr >> 4) + (rr & 15)) * ldc + pnl * BM + cc * 16;
; #pragma unroll
;         for (int ai = 0; ai < 2; ++ai)
; #pragma unroll
;             for (int mp = 0; mp < 2; ++mp) {
; #pragma unroll
;                 for (int ms = 0; ms < 2; ++ms)
; #pragma unroll
;                     for (int bj = 0; bj < 2; ++bj) { const int m = 2 * mp + ms; const f32x4 v0 = acc[ai][bj][m][0] * scale + bv[bj][0], v1 = acc[ai][bj][m][1] * scale + bv[bj][1];
;                         u32x2 w; w.x = pk4_fp8(v0[0], v0[1], v0[2], v0[3]); w.y = pk4_fp8(v1[0], v1[1], v1[2], v1[3]);
;                         *(LAS u32x2*)(wp + ms * SLAB + 128 * bj) = w; }
.LBB0_1150:
	s_ashr_i32 s2, s21, 31
	s_lshr_b32 s2, s2, 29
	s_add_i32 s2, s21, s2
	s_ashr_i32 s2, s2, 3
	s_lshl_b32 s3, s2, 11
	s_lshl_b32 s21, s21, 8
	v_readlane_b32 s56, v254, 0
	s_sub_i32 s22, s21, s3
	s_ashr_i32 s3, s2, 31
	v_readlane_b32 s60, v254, 4
	v_readlane_b32 s61, v254, 5
	s_lshl_b64 s[2:3], s[2:3], 13
	v_readlane_b32 s62, v254, 6
	v_readlane_b32 s63, v254, 7
	s_mov_b64 s[24:25], s[60:61]
	v_or_b32_e32 v2, s22, v186
	s_add_u32 s2, s24, s2
	s_addc_u32 s3, s25, s3
	v_ashrrev_i32_e32 v3, 31, v2
	s_nop 15
	s_nop 15
	v_lshl_add_u64 v[2:3], v[2:3], 2, s[2:3]
	global_load_dwordx4 v[14:17], v[2:3], off
	global_load_dwordx4 v[10:13], v[2:3], off offset:16
	global_load_dwordx4 v[6:9], v[2:3], off offset:512
	s_nop 0
	global_load_dwordx4 v[2:5], v[2:3], off offset:528
	v_mov_b32_e32 v20, 0
	v_mov_b32_e32 v21, 0
	v_mov_b32_e32 v22, 0
	v_mov_b32_e32 v23, 0
	v_mov_b32_e32 v24, 0
	v_mov_b32_e32 v25, 0
	v_mov_b32_e32 v26, 0
	v_mov_b32_e32 v27, 0
	v_lshl_or_b32 v18, s20, 8, v187
	v_add_u32_e32 v178, 0x2000, v188
	v_ashrrev_i32_e32 v19, 31, v18
	v_lshlrev_b64 v[18:19], 11, v[18:19]
	v_mov_b32_e32 v32, 0
	v_mov_b32_e32 v33, 0
	v_lshl_add_u64 v[18:19], s[4:5], 0, v[18:19]
	s_ashr_i32 s23, s22, 31
	v_lshl_add_u64 v[18:19], v[18:19], 0, s[22:23]
	v_lshl_add_u64 v[18:19], v[18:19], 0, v[170:171]
	v_add_co_u32_e32 v176, vcc, s50, v18
	v_mov_b32_e32 v28, 0
	v_mov_b32_e32 v29, 0
	v_mov_b32_e32 v30, 0
	v_mov_b32_e32 v31, 0
	v_addc_co_u32_e32 v177, vcc, 0, v19, vcc
	s_cmp_eq_u32 s49, s48
	s_mov_b64 s[2:3], -1
	v_readlane_b32 s57, v254, 1
	v_readlane_b32 s58, v254, 2
	v_readlane_b32 s59, v254, 3
	s_mov_b64 s[26:27], s[62:63]
	s_waitcnt vmcnt(0)
	v_add_u32_e32 v232, 0xfffe7000, v188
	v_add_u32_e32 v233, 0xfffe9000, v188
	v_add_u32_e32 v234, 0xfffe7000, v189
	v_add_co_u32_e32 v236, vcc, 0x10000, v18
	s_nop 1
	v_addc_co_u32_e32 v237, vcc, 0, v19, vcc
	v_add_co_u32_e32 v238, vcc, 0x18000, v18
	s_nop 1
	v_addc_co_u32_e32 v239, vcc, 0, v19, vcc
	v_pk_fma_f32 v[158:159], v[158:159], s[12:13], v[14:15] op_sel_hi:[1,0,1]
	v_pk_fma_f32 v[160:161], v[160:161], s[12:13], v[16:17] op_sel_hi:[1,0,1]
	v_pk_fma_f32 v[154:155], v[154:155], s[12:13], v[10:11] op_sel_hi:[1,0,1]
	v_pk_fma_f32 v[156:157], v[156:157], s[12:13], v[12:13] op_sel_hi:[1,0,1]
	v_cvt_pk_fp8_f32 v20, v158, v159
	v_cvt_pk_fp8_f32 v20, v160, v161 op_sel:[0,0,1]
	v_cvt_pk_fp8_f32 v21, v154, v155
	v_cvt_pk_fp8_f32 v21, v156, v157 op_sel:[0,0,1]
	v_pk_fma_f32 v[138:139], v[138:139], s[12:13], v[6:7] op_sel_hi:[1,0,1]
	v_pk_fma_f32 v[140:141], v[140:141], s[12:13], v[8:9] op_sel_hi:[1,0,1]
	v_pk_fma_f32 v[130:131], v[130:131], s[12:13], v[2:3] op_sel_hi:[1,0,1]
	v_pk_fma_f32 v[132:133], v[132:133], s[12:13], v[4:5] op_sel_hi:[1,0,1]
	v_cvt_pk_fp8_f32 v22, v138, v139
	v_cvt_pk_fp8_f32 v22, v140, v141 op_sel:[0,0,1]
	v_cvt_pk_fp8_f32 v23, v130, v131
	v_cvt_pk_fp8_f32 v23, v132, v133 op_sel:[0,0,1]
	v_pk_fma_f32 v[150:151], v[150:151], s[12:13], v[14:15] op_sel_hi:[1,0,1]
	v_pk_fma_f32 v[152:153], v[152:153], s[12:13], v[16:17] op_sel_hi:[1,0,1]
	v_pk_fma_f32 v[146:147], v[146:147], s[12:13], v[10:11] op_sel_hi:[1,0,1]
	v_pk_fma_f32 v[148:149], v[148:149], s[12:13], v[12:13] op_sel_hi:[1,0,1]
	v_cvt_pk_fp8_f32 v24, v150, v151
	v_cvt_pk_fp8_f32 v24, v152, v153 op_sel:[0,0,1]
	v_cvt_pk_fp8_f32 v25, v146, v147
	v_cvt_pk_fp8_f32 v25, v148, v149 op_sel:[0,0,1]
	v_pk_fma_f32 v[126:127], v[126:127], s[12:13], v[6:7] op_sel_hi:[1,0,1]
	v_pk_fma_f32 v[128:129], v[128:129], s[12:13], v[8:9] op_sel_hi:[1,0,1]
	v_pk_fma_f32 v[122:123], v[122:123], s[12:13], v[2:3] op_sel_hi:[1,0,1]
	v_pk_fma_f32 v[124:125], v[124:125], s[12:13], v[4:5] op_sel_hi:[1,0,1]
	v_cvt_pk_fp8_f32 v26, v126, v127
	v_cvt_pk_fp8_f32 v26, v128, v129 op_sel:[0,0,1]
	v_cvt_pk_fp8_f32 v27, v122, v123
	v_cvt_pk_fp8_f32 v27, v124, v125 op_sel:[0,0,1]
	v_pk_fma_f32 v[142:143], v[142:143], s[12:13], v[14:15] op_sel_hi:[1,0,1]
	v_pk_fma_f32 v[144:145], v[144:145], s[12:13], v[16:17] op_sel_hi:[1,0,1]
	v_pk_fma_f32 v[134:135], v[134:135], s[12:13], v[10:11] op_sel_hi:[1,0,1]
	v_pk_fma_f32 v[136:137], v[136:137], s[12:13], v[12:13] op_sel_hi:[1,0,1]
	v_cvt_pk_fp8_f32 v224, v142, v143
	v_cvt_pk_fp8_f32 v224, v144, v145 op_sel:[0,0,1]
	v_cvt_pk_fp8_f32 v225, v134, v135
	v_cvt_pk_fp8_f32 v225, v136, v137 op_sel:[0,0,1]
	v_pk_fma_f32 v[118:119], v[118:119], s[12:13], v[6:7] op_sel_hi:[1,0,1]
	v_pk_fma_f32 v[120:121], v[120:121], s[12:13], v[8:9] op_sel_hi:[1,0,1]
	v_pk_fma_f32 v[114:115], v[114:115], s[12:13], v[2:3] op_sel_hi:[1,0,1]
	v_pk_fma_f32 v[116:117], v[116:117], s[12:13], v[4:5] op_sel_hi:[1,0,1]
	v_cvt_pk_fp8_f32 v226, v118, v119
	v_cvt_pk_fp8_f32 v226, v120, v121 op_sel:[0,0,1]
	v_cvt_pk_fp8_f32 v227, v114, v115
	v_cvt_pk_fp8_f32 v227, v116, v117 op_sel:[0,0,1]
	v_pk_fma_f32 v[110:111], v[110:111], s[12:13], v[14:15] op_sel_hi:[1,0,1]
	v_pk_fma_f32 v[112:113], v[112:113], s[12:13], v[16:17] op_sel_hi:[1,0,1]
	v_pk_fma_f32 v[106:107], v[106:107], s[12:13], v[10:11] op_sel_hi:[1,0,1]
	v_pk_fma_f32 v[108:109], v[108:109], s[12:13], v[12:13] op_sel_hi:[1,0,1]
	v_cvt_pk_fp8_f32 v228, v110, v111
	v_cvt_pk_fp8_f32 v228, v112, v113 op_sel:[0,0,1]
	v_cvt_pk_fp8_f32 v229, v106, v107
	v_cvt_pk_fp8_f32 v229, v108, v109 op_sel:[0,0,1]
	v_pk_fma_f32 v[102:103], v[102:103], s[12:13], v[6:7] op_sel_hi:[1,0,1]
	v_pk_fma_f32 v[104:105], v[104:105], s[12:13], v[8:9] op_sel_hi:[1,0,1]
	v_pk_fma_f32 v[98:99], v[98:99], s[12:13], v[2:3] op_sel_hi:[1,0,1]
	v_pk_fma_f32 v[100:101], v[100:101], s[12:13], v[4:5] op_sel_hi:[1,0,1]
	v_cvt_pk_fp8_f32 v230, v102, v103
	v_cvt_pk_fp8_f32 v230, v104, v105 op_sel:[0,0,1]
	v_cvt_pk_fp8_f32 v231, v98, v99
	v_cvt_pk_fp8_f32 v231, v100, v101 op_sel:[0,0,1]
	ds_write2_b64 v188, v[20:21], v[22:23] offset1:16
	ds_write2_b64 v178, v[24:25], v[26:27] offset0:64 offset1:80
	ds_write2_b64 v232, v[224:225], v[226:227] offset1:16
	ds_write2_b64 v233, v[228:229], v[230:231] offset0:64 offset1:80
	s_waitcnt lgkmcnt(0)
	s_barrier
; #define LAS __attribute__((address_space(3)))
; __device__ __forceinline__ unsigned pk4_fp8(float a, float b, float c, float d) { int w = 0; w = __builtin_amdgcn_cvt_pk_fp8_f32(a, b, w, false); w = __builtin_amdgcn_cvt_pk_fp8_f32(c, d, w, true); return (unsigned)w; }
;     __device__ __forceinline__ void operator()(const f32x4 (&acc)[2][2][4][2], const Unit& u, int wr, int wc, int fr, int fq) const {
;     ...
; #pragma unroll
;         for (int ai = 0; ai < 2; ++ai)
; #pragma unroll
;             for (int mp = 0; mp < 2; ++mp) {
; #pragma unroll
;                 for (int ms = 0; ms < 2; ++ms)
; #pragma unroll
;                     for (int bj = 0; bj < 2; ++bj) { const int m = 2 * mp + ms; const f32x4 v0 = acc[ai][bj][m][0] * scale + bv[bj][0], v1 = acc[ai][bj][m][1] * scale + bv[bj][1];
;                         u32x2 w; w.x = pk4_fp8(v0[0], v0[1], v0[2], v0[3]); w.y = pk4_fp8(v1[0], v1[1], v1[2], v1[3]);
;                         *(LAS u32x2*)(wp + ms * SLAB + 128 * bj) = w; }
;                 asm volatile("s_waitcnt lgkmcnt(0)" ::: "memory"); __builtin_amdgcn_s_barrier(); asm volatile("" ::: "memory");
; #pragma unroll
;                 for (int ms = 0; ms < 2; ++ms) *(u32x4*)(gp + (size_t)(ai * HALF + (2 * mp + ms) * 16) * ldc) = *(const LAS u32x4*)(rp + ms * SLAB);
;                 asm volatile("s_waitcnt lgkmcnt(0)" ::: "memory"); __builtin_amdgcn_s_barrier(); asm volatile("" ::: "memory");
;             }
	ds_read_b128 v[20:23], v189
	ds_read_b128 v[24:27], v189 offset:8704
	ds_read_b128 v[224:227], v234
	ds_read_b128 v[228:231], v234 offset:8704
	s_waitcnt lgkmcnt(3)
	global_store_dwordx4 v[18:19], v[20:23], off
	s_waitcnt lgkmcnt(2)
	global_store_dwordx4 v[176:177], v[24:27], off
	s_waitcnt lgkmcnt(1)
	global_store_dwordx4 v[236:237], v[224:227], off
	s_waitcnt lgkmcnt(0)
	global_store_dwordx4 v[238:239], v[228:231], off
	s_barrier
	v_add_co_u32_e32 v18, vcc, 0x40000, v18
	s_nop 1
	v_addc_co_u32_e32 v19, vcc, 0, v19, vcc
	v_add_co_u32_e32 v176, vcc, 0x40000, v176
	s_nop 1
	v_addc_co_u32_e32 v177, vcc, 0, v177, vcc
	v_add_co_u32_e32 v236, vcc, 0x40000, v236
	s_nop 1
	v_addc_co_u32_e32 v237, vcc, 0, v237, vcc
	v_add_co_u32_e32 v238, vcc, 0x40000, v238
	s_nop 1
	v_addc_co_u32_e32 v239, vcc, 0, v239, vcc
	v_pk_fma_f32 v[94:95], v[94:95], s[12:13], v[14:15] op_sel_hi:[1,0,1]
	v_pk_fma_f32 v[96:97], v[96:97], s[12:13], v[16:17] op_sel_hi:[1,0,1]
	v_pk_fma_f32 v[90:91], v[90:91], s[12:13], v[10:11] op_sel_hi:[1,0,1]
	v_pk_fma_f32 v[92:93], v[92:93], s[12:13], v[12:13] op_sel_hi:[1,0,1]
	v_cvt_pk_fp8_f32 v20, v94, v95
	v_cvt_pk_fp8_f32 v20, v96, v97 op_sel:[0,0,1]
	v_cvt_pk_fp8_f32 v21, v90, v91
	v_cvt_pk_fp8_f32 v21, v92, v93 op_sel:[0,0,1]
	v_pk_fma_f32 v[82:83], v[82:83], s[12:13], v[6:7] op_sel_hi:[1,0,1]
	v_pk_fma_f32 v[84:85], v[84:85], s[12:13], v[8:9] op_sel_hi:[1,0,1]
	v_pk_fma_f32 v[74:75], v[74:75], s[12:13], v[2:3] op_sel_hi:[1,0,1]
	v_pk_fma_f32 v[76:77], v[76:77], s[12:13], v[4:5] op_sel_hi:[1,0,1]
	v_cvt_pk_fp8_f32 v22, v82, v83
	v_cvt_pk_fp8_f32 v22, v84, v85 op_sel:[0,0,1]
	v_cvt_pk_fp8_f32 v23, v74, v75
	v_cvt_pk_fp8_f32 v23, v76, v77 op_sel:[0,0,1]
	v_pk_fma_f32 v[86:87], v[86:87], s[12:13], v[14:15] op_sel_hi:[1,0,1]
	v_pk_fma_f32 v[88:89], v[88:89], s[12:13], v[16:17] op_sel_hi:[1,0,1]
	v_pk_fma_f32 v[78:79], v[78:79], s[12:13], v[10:11] op_sel_hi:[1,0,1]
	v_pk_fma_f32 v[80:81], v[80:81], s[12:13], v[12:13] op_sel_hi:[1,0,1]
	v_cvt_pk_fp8_f32 v24, v86, v87
	v_cvt_pk_fp8_f32 v24, v88, v89 op_sel:[0,0,1]
	v_cvt_pk_fp8_f32 v25, v78, v79
	v_cvt_pk_fp8_f32 v25, v80, v81 op_sel:[0,0,1]
	v_pk_fma_f32 v[70:71], v[70:71], s[12:13], v[6:7] op_sel_hi:[1,0,1]
	v_pk_fma_f32 v[72:73], v[72:73], s[12:13], v[8:9] op_sel_hi:[1,0,1]
	v_pk_fma_f32 v[66:67], v[66:67], s[12:13], v[2:3] op_sel_hi:[1,0,1]
	v_pk_fma_f32 v[68:69], v[68:69], s[12:13], v[4:5] op_sel_hi:[1,0,1]
	v_cvt_pk_fp8_f32 v26, v70, v71
	v_cvt_pk_fp8_f32 v26, v72, v73 op_sel:[0,0,1]
	v_cvt_pk_fp8_f32 v27, v66, v67
	v_cvt_pk_fp8_f32 v27, v68, v69 op_sel:[0,0,1]
	v_pk_fma_f32 v[62:63], v[62:63], s[12:13], v[14:15] op_sel_hi:[1,0,1]
	v_pk_fma_f32 v[64:65], v[64:65], s[12:13], v[16:17] op_sel_hi:[1,0,1]
	v_pk_fma_f32 v[58:59], v[58:59], s[12:13], v[10:11] op_sel_hi:[1,0,1]
	v_pk_fma_f32 v[60:61], v[60:61], s[12:13], v[12:13] op_sel_hi:[1,0,1]
	v_cvt_pk_fp8_f32 v224, v62, v63
	v_cvt_pk_fp8_f32 v224, v64, v65 op_sel:[0,0,1]
	v_cvt_pk_fp8_f32 v225, v58, v59
	v_cvt_pk_fp8_f32 v225, v60, v61 op_sel:[0,0,1]
	v_pk_fma_f32 v[50:51], v[50:51], s[12:13], v[6:7] op_sel_hi:[1,0,1]
	v_pk_fma_f32 v[52:53], v[52:53], s[12:13], v[8:9] op_sel_hi:[1,0,1]
	v_pk_fma_f32 v[42:43], v[42:43], s[12:13], v[2:3] op_sel_hi:[1,0,1]
	v_pk_fma_f32 v[44:45], v[44:45], s[12:13], v[4:5] op_sel_hi:[1,0,1]
	v_cvt_pk_fp8_f32 v226, v50, v51
	v_cvt_pk_fp8_f32 v226, v52, v53 op_sel:[0,0,1]
	v_cvt_pk_fp8_f32 v227, v42, v43
	v_cvt_pk_fp8_f32 v227, v44, v45 op_sel:[0,0,1]
	v_pk_fma_f32 v[54:55], v[54:55], s[12:13], v[14:15] op_sel_hi:[1,0,1]
	v_pk_fma_f32 v[56:57], v[56:57], s[12:13], v[16:17] op_sel_hi:[1,0,1]
	v_pk_fma_f32 v[46:47], v[46:47], s[12:13], v[10:11] op_sel_hi:[1,0,1]
	v_pk_fma_f32 v[48:49], v[48:49], s[12:13], v[12:13] op_sel_hi:[1,0,1]
	v_cvt_pk_fp8_f32 v228, v54, v55
	v_cvt_pk_fp8_f32 v228, v56, v57 op_sel:[0,0,1]
	v_cvt_pk_fp8_f32 v229, v46, v47
	v_cvt_pk_fp8_f32 v229, v48, v49 op_sel:[0,0,1]
	v_pk_fma_f32 v[38:39], v[38:39], s[12:13], v[6:7] op_sel_hi:[1,0,1]
	v_pk_fma_f32 v[40:41], v[40:41], s[12:13], v[8:9] op_sel_hi:[1,0,1]
	v_pk_fma_f32 v[34:35], v[34:35], s[12:13], v[2:3] op_sel_hi:[1,0,1]
	v_pk_fma_f32 v[36:37], v[36:37], s[12:13], v[4:5] op_sel_hi:[1,0,1]
	v_cvt_pk_fp8_f32 v230, v38, v39
	v_cvt_pk_fp8_f32 v230, v40, v41 op_sel:[0,0,1]
	v_cvt_pk_fp8_f32 v231, v34, v35
	v_cvt_pk_fp8_f32 v231, v36, v37 op_sel:[0,0,1]
	ds_write2_b64 v188, v[20:21], v[22:23] offset1:16
	ds_write2_b64 v178, v[24:25], v[26:27] offset0:64 offset1:80
	ds_write2_b64 v232, v[224:225], v[226:227] offset1:16
	ds_write2_b64 v233, v[228:229], v[230:231] offset0:64 offset1:80
	s_waitcnt lgkmcnt(0)
	s_barrier
	ds_read_b128 v[20:23], v189
	ds_read_b128 v[24:27], v189 offset:8704
	ds_read_b128 v[224:227], v234
	ds_read_b128 v[228:231], v234 offset:8704
	s_waitcnt lgkmcnt(3)
	global_store_dwordx4 v[18:19], v[20:23], off
	s_waitcnt lgkmcnt(2)
	global_store_dwordx4 v[176:177], v[24:27], off
	s_waitcnt lgkmcnt(1)
	global_store_dwordx4 v[236:237], v[224:227], off
	s_waitcnt lgkmcnt(0)
	global_store_dwordx4 v[238:239], v[228:231], off
	s_barrier
	s_cbranch_scc1 .LBB0_1143
	s_andn2_b64 vcc, exec, s[0:1]
	s_cbranch_vccnz .LBB0_1142
	s_barrier
	s_branch .LBB0_1142
